# attention block-importance assembly: the 64 per-key LDS reads issued once up front instead of 16 dependent read-wait rounds
# speedup vs baseline: 1.0049x; 1.0049x over previous
; #define LAS __attribute__((address_space(3)))
; #define ATT_WAIT_BAR() asm volatile("s_waitcnt vmcnt(0) lgkmcnt(0)\n\ts_barrier" ::: "memory")
; __device__ __forceinline__ int opq_v(int x) { asm volatile("" : "+v"(x)); return x; }
; __device__ __forceinline__ void att_unit_mfma(KArgs args, int b, int qb, LAS unsigned char* lds, int wave0, int lane0, int tid0) {
;     ...
;         ATT_WAIT_BAR();
;         { ATT_IDS const char* ksb0 = (const char*)(z + (size_t)(b * SEQ) * ZP + ZC_KS + g * 64);
;           const char* kp0 = ksb0 + (size_t)(64 * qb) * ZPB; att_stage(lds, 0, kp0, kp0 + (ZC_VS - ZC_KS) * 2, ZPB, wave, lane);
;           const char* kp1 = ksb0 + (size_t)(64 * (qb > 0 ? qb - 1 : 0)) * ZPB; att_stage(lds, 1, kp1, kp1 + (ZC_VS - ZC_KS) * 2, ZPB, wave, lane); }
;         { const int tid = opq_v(tid0); const int stok = tid >> 3, e8 = tid & 7; const LAS float* ilc = (const LAS float*)(lds + ATT_SC);
;           unsigned key[8];
; #pragma unroll
;           for (int k = 0; k < 8; ++k) { const int j = 8 * e8 + k; const float v = imp[(0 * 64 + stok) * 65 + j] * ilc[stok] + imp[(1 * 64 + stok) * 65 + j] * ilc[64 + stok] + imp[(2 * 64 + stok) * 65 + j] * ilc[128 + stok] + imp[(3 * 64 + stok) * 65 + j] * ilc[192 + stok];
;               const bool valid = j <= qb, forced = valid && (j == 0 || j == qb || j == qb - 1);
;               const unsigned bits_ = __builtin_bit_cast(unsigned, forced ? 1e30f : (valid ? v : -1e30f));
;               key[k] = ((bits_ ^ ((bits_ >> 31) ? 0xFFFFFFFFu : 0x80000000u)) & ~63u) | (unsigned)(63 - j); }
.LBB0_590:
	s_lshl_b32 s0, s36, 6
	s_xor_b64 s[16:17], s[48:49], -1
	v_mov_b32_e32 v1, v174
	s_lshl_b32 s0, s0, 1
	v_readlane_b32 s1, v255, 26
	s_waitcnt vmcnt(0) lgkmcnt(0)
	s_barrier
	s_mov_b32 s4, s69
	s_add_u32 s70, s1, s0
	v_readlane_b32 s0, v255, 28
	v_ashrrev_i32_e32 v8, 3, v1
	s_addc_u32 s71, s0, 0
	s_mul_i32 s0, s2, 0x50000
	v_lshl_add_u32 v10, s4, 3, v8
	s_add_u32 s0, s70, s0
	s_mul_hi_i32 s1, s3, 0x1400
	v_lshrrev_b32_e32 v4, 1, v10
	s_addc_u32 s1, s71, s1
	v_and_b32_e32 v9, 7, v1
	v_xor_b32_e32 v1, v4, v1
	v_mov_b64_e32 v[2:3], s[0:1]
	v_lshlrev_b32_e32 v1, 4, v1
	v_mad_i64_i32 v[2:3], s[0:1], v10, s88, v[2:3]
	v_and_b32_e32 v4, 0x70, v1
	v_lshlrev_b32_e32 v1, 1, v8
	v_mov_b32_e32 v5, v0
	v_bitop3_b32 v1, v1, v9, 6 bitop3:0x6c
	s_lshl_b32 s0, s4, 10
	s_waitcnt vmcnt(0)
	v_lshl_add_u64 v[6:7], v[2:3], 0, v[4:5]
	s_mov_b64 s[6:7], 0xe00
	v_lshlrev_b32_e32 v8, 4, v1
	v_mov_b32_e32 v9, v0
	s_add_i32 s4, s0, 0
	v_lshl_add_u64 v[6:7], v[6:7], 0, s[6:7]
	v_lshl_add_u64 v[2:3], v[2:3], 0, v[8:9]
	s_mov_b64 s[8:9], 0xf00
	s_add_i32 s0, s4, 0x2000
	s_mov_b32 s1, m0
	s_mov_b32 m0, s4
	s_nop 0
	global_load_lds_dwordx4 v[6:7], off
	s_mov_b32 m0, s1
	v_lshl_add_u64 v[2:3], v[2:3], 0, s[8:9]
	s_mov_b32 s1, m0
	s_mov_b32 m0, s0
	s_nop 0
	global_load_lds_dwordx4 v[2:3], off
	s_mov_b32 m0, s1
	v_readlane_b32 s0, v255, 52
	s_add_u32 s0, s70, s0
	v_readlane_b32 s1, v255, 51
	s_addc_u32 s1, s71, s1
	v_mov_b32_e32 v1, v175
	v_mov_b64_e32 v[2:3], s[0:1]
	v_mad_i64_i32 v[2:3], s[0:1], v10, s88, v[2:3]
	v_lshl_add_u64 v[4:5], v[2:3], 0, v[4:5]
	v_lshl_add_u64 v[4:5], v[4:5], 0, s[6:7]
	v_lshl_add_u64 v[2:3], v[2:3], 0, v[8:9]
	s_add_i32 s0, s4, 0x4000
	s_mov_b32 s1, m0
	s_mov_b32 m0, s0
	s_nop 0
	global_load_lds_dwordx4 v[4:5], off
	s_mov_b32 m0, s1
	v_lshl_add_u64 v[2:3], v[2:3], 0, s[8:9]
	s_addk_i32 s4, 0x6000
	s_mov_b32 s0, m0
	s_mov_b32 m0, s4
	s_nop 0
	global_load_lds_dwordx4 v[2:3], off
	s_mov_b32 m0, s0
	s_mov_b64 s[80:81], 0xe00
	v_ashrrev_i32_e32 v4, 3, v1
	v_and_b32_e32 v2, 7, v1
	v_mul_lo_u32 v5, v4, s56
	v_lshlrev_b32_e32 v3, 3, v2
	v_add_u32_e32 v11, s37, v5
	v_lshl_add_u32 v7, v4, 2, s91
	s_mov_b64 s[96:97], 0xf00
	v_add_u32_e32 v12, 0x4100, v11
	v_add_u32_e32 v8, 0x100, v7
	v_add_u32_e32 v13, 0x8200, v11
	v_add_u32_e32 v5, 0x200, v7
	v_add_u32_e32 v16, 0xc300, v11
	v_add_u32_e32 v6, 0x300, v7
	v_cmp_ge_i32_e32 vcc, s2, v3
	v_mov_b32_e32 v4, 0xf149f2ca
	v_lshlrev_b32_e32 v17, 2, v3
	v_mov_b32_e32 v9, 0xf149f2ca
	v_add_u32_e32 v86, v11, v17
	v_add_u32_e32 v87, v12, v17
	v_add_u32_e32 v88, v13, v17
	v_add_u32_e32 v89, v16, v17
	ds_read_b32 v50, v86
	ds_read_b32 v51, v86 offset:4
	ds_read_b32 v52, v86 offset:8
	ds_read_b32 v53, v86 offset:12
	ds_read_b32 v54, v86 offset:16
	ds_read_b32 v55, v86 offset:20
	ds_read_b32 v56, v86 offset:24
	ds_read_b32 v57, v86 offset:28
	ds_read_b32 v58, v87
	ds_read_b32 v59, v87 offset:4
	ds_read_b32 v60, v87 offset:8
	ds_read_b32 v61, v87 offset:12
	ds_read_b32 v62, v87 offset:16
	ds_read_b32 v63, v87 offset:20
	ds_read_b32 v64, v87 offset:24
	ds_read_b32 v65, v87 offset:28
	ds_read_b32 v66, v88
	ds_read_b32 v67, v88 offset:4
	ds_read_b32 v68, v88 offset:8
	ds_read_b32 v69, v88 offset:12
	ds_read_b32 v70, v88 offset:16
	ds_read_b32 v71, v88 offset:20
	ds_read_b32 v72, v88 offset:24
	ds_read_b32 v73, v88 offset:28
	ds_read_b32 v74, v89
	ds_read_b32 v75, v89 offset:4
	ds_read_b32 v76, v89 offset:8
	ds_read_b32 v77, v89 offset:12
	ds_read_b32 v78, v89 offset:16
	ds_read_b32 v79, v89 offset:20
	ds_read_b32 v80, v89 offset:24
	ds_read_b32 v81, v89 offset:28
	ds_read_b32 v82, v7
	ds_read_b32 v83, v8
	ds_read_b32 v84, v5
	ds_read_b32 v85, v6
	s_waitcnt lgkmcnt(0)
	s_and_saveexec_b64 s[6:7], vcc
	s_cbranch_execz .LBB0_592
	v_add_u32_e32 v9, v11, v17
	v_mov_b32_e32 v14, v50
	v_mov_b32_e32 v18, v82
	v_add_u32_e32 v9, v12, v17
	v_mov_b32_e32 v15, v58
	v_mov_b32_e32 v19, v83
	v_add_u32_e32 v9, v13, v17
	v_cmp_eq_u32_e32 vcc, 0, v2
	v_cmp_eq_u32_e64 s[4:5], s2, v3
	s_or_b64 s[0:1], vcc, s[4:5]
	s_waitcnt lgkmcnt(0)
	v_mul_f32_e32 v10, v15, v19
	v_pk_fma_f32 v[14:15], v[14:15], v[18:19], v[10:11] op_sel_hi:[1,1,0]
	v_mov_b32_e32 v18, v66
	v_mov_b32_e32 v20, v84
	v_add_u32_e32 v9, v16, v17
	v_mov_b32_e32 v19, v74
	v_mov_b32_e32 v21, v85
	v_cmp_eq_u32_e32 vcc, s46, v3
	s_or_b64 vcc, s[0:1], vcc
	s_waitcnt lgkmcnt(0)
	v_pk_fma_f32 v[14:15], v[18:19], v[20:21], v[14:15]
	v_mul_f32_e32 v10, v19, v21
	v_pk_add_f32 v[14:15], v[14:15], v[10:11] op_sel_hi:[1,0]
	s_nop 0
	v_cndmask_b32_e32 v9, v14, v214, vcc
.LBB0_592:
	s_or_b64 exec, exec, s[6:7]
	v_or_b32_e32 v10, 1, v3
	v_cmp_gt_i32_e32 vcc, s2, v3
	v_add_u32_e32 v15, v11, v17
	v_add_u32_e32 v14, v12, v17
	v_add_u32_e32 v12, v13, v17
	v_add_u32_e32 v11, v16, v17
	s_and_saveexec_b64 s[6:7], vcc
	s_cbranch_execz .LBB0_594
	v_mov_b32_e32 v16, v51
	v_mov_b32_e32 v18, v82
	v_mov_b32_e32 v17, v59
	v_mov_b32_e32 v19, v83
	v_cmp_eq_u32_e32 vcc, s2, v10
	v_cmp_eq_u32_e64 s[4:5], s46, v10
	s_or_b64 vcc, vcc, s[4:5]
	s_waitcnt lgkmcnt(0)
	v_mul_f32_e32 v4, v17, v19
	v_pk_fma_f32 v[16:17], v[16:17], v[18:19], v[4:5] op_sel_hi:[1,1,0]
	v_mov_b32_e32 v18, v67
	v_mov_b32_e32 v20, v84
	v_mov_b32_e32 v19, v75
	v_mov_b32_e32 v21, v85
	s_waitcnt lgkmcnt(0)
	v_pk_fma_f32 v[16:17], v[18:19], v[20:21], v[16:17]
	v_mul_f32_e32 v4, v19, v21
	v_pk_add_f32 v[16:17], v[16:17], v[4:5] op_sel_hi:[1,0]
	s_nop 0
	v_cndmask_b32_e32 v4, v16, v214, vcc
; __device__ __forceinline__ void att_unit_mfma(KArgs args, int b, int qb, LAS unsigned char* lds, int wave0, int lane0, int tid0) {
;     ...
;           for (int k = 0; k < 8; ++k) { const int j = 8 * e8 + k; const float v = imp[(0 * 64 + stok) * 65 + j] * ilc[stok] + imp[(1 * 64 + stok) * 65 + j] * ilc[64 + stok] + imp[(2 * 64 + stok) * 65 + j] * ilc[128 + stok] + imp[(3 * 64 + stok) * 65 + j] * ilc[192 + stok];
;               const bool valid = j <= qb, forced = valid && (j == 0 || j == qb || j == qb - 1);
;               const unsigned bits_ = __builtin_bit_cast(unsigned, forced ? 1e30f : (valid ? v : -1e30f));
;               key[k] = ((bits_ ^ ((bits_ >> 31) ? 0xFFFFFFFFu : 0x80000000u)) & ~63u) | (unsigned)(63 - j); }
.LBB0_594:
	s_or_b64 exec, exec, s[6:7]
	v_or_b32_e32 v13, 2, v3
	v_cmp_ge_i32_e32 vcc, s2, v13
	v_mov_b32_e32 v17, 0xf149f2ca
	v_mov_b32_e32 v16, 0xf149f2ca
	s_and_saveexec_b64 s[6:7], vcc
	s_cbranch_execz .LBB0_596
	v_mov_b32_e32 v18, v52
	v_mov_b32_e32 v20, v82
	v_mov_b32_e32 v19, v60
	v_mov_b32_e32 v21, v83
	v_cmp_eq_u32_e32 vcc, s2, v13
	v_cmp_eq_u32_e64 s[4:5], s46, v13
	s_or_b64 vcc, vcc, s[4:5]
	s_waitcnt lgkmcnt(0)
	v_mul_f32_e32 v16, v19, v21
	v_pk_fma_f32 v[18:19], v[18:19], v[20:21], v[16:17] op_sel_hi:[1,1,0]
	v_mov_b32_e32 v20, v68
	v_mov_b32_e32 v22, v84
	v_mov_b32_e32 v21, v76
	v_mov_b32_e32 v23, v85
	s_waitcnt lgkmcnt(0)
	v_pk_fma_f32 v[18:19], v[20:21], v[22:23], v[18:19]
	v_mul_f32_e32 v16, v21, v23
	v_pk_add_f32 v[18:19], v[18:19], v[16:17] op_sel_hi:[1,0]
	s_nop 0
	v_cndmask_b32_e32 v16, v18, v214, vcc
.LBB0_596:
	s_or_b64 exec, exec, s[6:7]
	v_or_b32_e32 v18, 3, v3
	v_cmp_ge_i32_e32 vcc, s2, v18
	s_and_saveexec_b64 s[6:7], vcc
	s_cbranch_execz .LBB0_598
	v_mov_b32_e32 v20, v53
	v_mov_b32_e32 v22, v82
	v_mov_b32_e32 v21, v61
	v_mov_b32_e32 v23, v83
	v_cmp_eq_u32_e32 vcc, s2, v18
	v_cmp_eq_u32_e64 s[4:5], s46, v18
	s_or_b64 vcc, vcc, s[4:5]
	s_waitcnt lgkmcnt(0)
	v_mul_f32_e32 v24, v21, v23
	v_pk_fma_f32 v[20:21], v[20:21], v[22:23], v[24:25] op_sel_hi:[1,1,0]
	v_mov_b32_e32 v22, v69
	v_mov_b32_e32 v24, v84
	v_mov_b32_e32 v23, v77
	v_mov_b32_e32 v25, v85
	s_waitcnt lgkmcnt(0)
	v_pk_fma_f32 v[20:21], v[22:23], v[24:25], v[20:21]
	v_mul_f32_e32 v22, v23, v25
	v_pk_add_f32 v[20:21], v[20:21], v[22:23] op_sel_hi:[1,0]
	s_nop 0
	v_cndmask_b32_e32 v17, v20, v214, vcc
.LBB0_598:
	s_or_b64 exec, exec, s[6:7]
	v_or_b32_e32 v19, 4, v3
	v_cmp_ge_i32_e32 vcc, s2, v19
	v_mov_b32_e32 v21, 0xf149f2ca
	v_mov_b32_e32 v20, 0xf149f2ca
	s_and_saveexec_b64 s[6:7], vcc
	s_cbranch_execz .LBB0_600
	v_mov_b32_e32 v22, v54
	v_mov_b32_e32 v24, v82
	v_mov_b32_e32 v23, v62
	v_mov_b32_e32 v25, v83
	v_cmp_eq_u32_e32 vcc, s2, v19
	v_cmp_eq_u32_e64 s[4:5], s46, v19
	s_or_b64 vcc, vcc, s[4:5]
	s_waitcnt lgkmcnt(0)
	v_mul_f32_e32 v20, v23, v25
	v_pk_fma_f32 v[22:23], v[22:23], v[24:25], v[20:21] op_sel_hi:[1,1,0]
	v_mov_b32_e32 v24, v70
	v_mov_b32_e32 v26, v84
	v_mov_b32_e32 v25, v78
	v_mov_b32_e32 v27, v85
	s_waitcnt lgkmcnt(0)
	v_pk_fma_f32 v[22:23], v[24:25], v[26:27], v[22:23]
	v_mul_f32_e32 v20, v25, v27
	v_pk_add_f32 v[22:23], v[22:23], v[20:21] op_sel_hi:[1,0]
	s_nop 0
	v_cndmask_b32_e32 v20, v22, v214, vcc
.LBB0_600:
	s_or_b64 exec, exec, s[6:7]
	v_or_b32_e32 v22, 5, v3
	v_cmp_ge_i32_e32 vcc, s2, v22
	s_and_saveexec_b64 s[6:7], vcc
	s_cbranch_execz .LBB0_602
	v_mov_b32_e32 v24, v55
	v_mov_b32_e32 v26, v82
	v_mov_b32_e32 v25, v63
	v_mov_b32_e32 v27, v83
	v_cmp_eq_u32_e32 vcc, s2, v22
	v_cmp_eq_u32_e64 s[4:5], s46, v22
	s_or_b64 vcc, vcc, s[4:5]
	s_waitcnt lgkmcnt(0)
	v_mul_f32_e32 v28, v25, v27
	v_pk_fma_f32 v[24:25], v[24:25], v[26:27], v[28:29] op_sel_hi:[1,1,0]
	v_mov_b32_e32 v26, v71
	v_mov_b32_e32 v28, v84
	v_mov_b32_e32 v27, v79
	v_mov_b32_e32 v29, v85
	s_waitcnt lgkmcnt(0)
	v_pk_fma_f32 v[24:25], v[26:27], v[28:29], v[24:25]
	v_mul_f32_e32 v26, v27, v29
	v_pk_add_f32 v[24:25], v[24:25], v[26:27] op_sel_hi:[1,0]
	s_nop 0
	v_cndmask_b32_e32 v21, v24, v214, vcc
.LBB0_602:
	s_or_b64 exec, exec, s[6:7]
	v_or_b32_e32 v23, 6, v3
	v_cmp_ge_i32_e32 vcc, s2, v23
	v_mov_b32_e32 v24, 0xf149f2ca
	v_mov_b32_e32 v26, 0xf149f2ca
	s_and_saveexec_b64 s[6:7], vcc
	s_cbranch_execz .LBB0_604
	v_mov_b32_e32 v26, v56
	v_mov_b32_e32 v28, v82
	v_mov_b32_e32 v27, v64
	v_mov_b32_e32 v29, v83
	v_cmp_eq_u32_e32 vcc, s2, v23
	v_cmp_eq_u32_e64 s[4:5], s46, v23
	s_or_b64 vcc, vcc, s[4:5]
	s_waitcnt lgkmcnt(0)
	v_mul_f32_e32 v30, v27, v29
	v_pk_fma_f32 v[26:27], v[26:27], v[28:29], v[30:31] op_sel_hi:[1,1,0]
	v_mov_b32_e32 v28, v72
	v_mov_b32_e32 v30, v84
	v_mov_b32_e32 v29, v80
	v_mov_b32_e32 v31, v85
	s_waitcnt lgkmcnt(0)
	v_pk_fma_f32 v[26:27], v[28:29], v[30:31], v[26:27]
	v_mul_f32_e32 v28, v29, v31
	v_pk_add_f32 v[26:27], v[26:27], v[28:29] op_sel_hi:[1,0]
	s_nop 0
	v_cndmask_b32_e32 v26, v26, v214, vcc
.LBB0_604:
	s_or_b64 exec, exec, s[6:7]
	v_or_b32_e32 v25, 7, v3
	v_cmp_ge_i32_e32 vcc, s2, v25
	s_and_saveexec_b64 s[6:7], vcc
	s_cbranch_execz .LBB0_606
	v_mov_b32_e32 v28, v57
	v_mov_b32_e32 v30, v82
	v_mov_b32_e32 v29, v65
	v_mov_b32_e32 v31, v83
	v_cmp_eq_u32_e32 vcc, s2, v25
	v_cmp_eq_u32_e64 s[4:5], s46, v25
	s_or_b64 vcc, vcc, s[4:5]
	s_waitcnt lgkmcnt(0)
	v_mul_f32_e32 v8, v29, v31
	v_pk_fma_f32 v[14:15], v[28:29], v[30:31], v[8:9] op_sel_hi:[1,1,0]
	v_mov_b32_e32 v28, v73
	v_mov_b32_e32 v30, v84
	v_mov_b32_e32 v29, v81
	v_mov_b32_e32 v31, v85
	s_waitcnt lgkmcnt(0)
	v_pk_fma_f32 v[6:7], v[28:29], v[30:31], v[14:15]
	v_mul_f32_e32 v8, v29, v31
	v_pk_add_f32 v[6:7], v[6:7], v[8:9] op_sel_hi:[1,0]
	s_nop 0
	v_cndmask_b32_e32 v24, v6, v214, vcc
